# v17 plus two more exact changes: GEMM phase prologues issue the second LDS-DMA batch before the first wait; radix level 0 skipped when all candidates share its digit
# baseline (speedup 1.0000x reference)
; #define PG8_STAGE(bufoff, gbase, voff) do { _Pragma("unroll") for (int _i = 0; _i < 2; ++_i) \
;         __builtin_amdgcn_global_load_lds((const unsigned*)((const char*)(gbase) + (voff)[_i]), (LAS unsigned*)(lds + (bufoff) + ldsw + _i * 8192), 16, 0, 0); } while (0)
; #define PG8_WAIT_V(n) asm volatile("s_waitcnt vmcnt(" #n ")" ::: "memory")
; #define PG8_BAR __builtin_amdgcn_s_barrier()
; template <class Epi, class Sched, bool ALIGN_EPI = false, bool SP2 = false, bool FP8 = false  ,
;           bool GATHER = false  >
; __device__ __forceinline__ void gemm_phase(LAS unsigned char* lds, const Dims g, const Sched& S, const Epi& E, int tid_in) {
;     ...
;     const unsigned ldsw = (unsigned)wid * 1024u;
;     const int aoff0 = lds_byte(wr * 64 + fr, fq * 8), aoff1 = aoff0 + 1024;
;     const int boff0 = lds_byte(wc * 32 + fr, fq * 8), boff1 = boff0 + 1024;
;     ...
;         PG8_STAGE(PG8_SB(0, 0), cB, voffB); PG8_STAGE(PG8_SB(0, 1), cB + hstepB, voffB); PG8_STAGE_A(PG8_SA(0, 0), cA, 0, 0); PG8_STAGE_A(PG8_SA(0, 1), cA, 1, 0);
;         if (wr == 1) PG8_BAR;
;         PG8_WAIT_V(2); PG8_BAR;
;         PG8_STAGE(PG8_SB(1, 0), cB + kstep, voffB); PG8_STAGE_A(PG8_SA(1, 0), cA + kstep, 0, 0); PG8_STAGE(PG8_SB(1, 1), cB + hstepB + kstep, voffB);
;         PG8_WAIT_V(6); PG8_BAR;
.LBB0_315:
	s_add_u32 s46, s5, 0x36a00000
	s_addc_u32 s47, s4, 0
	s_add_i32 s13, s8, 0x18000
	s_add_u32 s14, s26, 0x40080
	s_addc_u32 s15, s27, 0
	s_add_i32 s48, s13, s12
	s_mov_b64 s[4:5], 0x80
	v_lshl_add_u64 v[6:7], v[6:7], 0, s[4:5]
	s_mov_b32 m0, s48
	s_add_i32 s49, s48, 0x2000
	global_load_lds_dwordx4 v[6:7], off
	v_lshl_add_u64 v[4:5], v[4:5], 0, s[4:5]
	s_mov_b32 m0, s49
	s_add_i32 s50, s42, 0x8000
	s_add_i32 s16, s8, 0x1c000
	global_load_lds_dwordx4 v[4:5], off
	v_lshl_add_u64 v[0:1], v[0:1], 0, s[4:5]
	s_mov_b32 m0, s50
	s_add_i32 s51, s42, 0xa000
	global_load_lds_dwordx4 v[0:1], off
	v_lshl_add_u64 v[0:1], v[2:3], 0, s[4:5]
	s_mov_b32 m0, s51
	s_add_i32 s52, s16, s12
	global_load_lds_dwordx4 v[0:1], off
	v_lshl_add_u64 v[0:1], s[14:15], 0, v[132:133]
	s_mov_b32 m0, s52
	s_add_i32 s53, s52, 0x2000
	global_load_lds_dwordx4 v[0:1], off
	v_lshl_add_u64 v[0:1], s[14:15], 0, v[128:129]
	s_mov_b32 m0, s53
	s_lshl_b32 s7, s7, 5
	global_load_lds_dwordx4 v[0:1], off
	s_waitcnt vmcnt(8)
	s_barrier
	v_lshrrev_b32_e32 v1, 1, v8
	v_and_b32_e32 v1, 24, v1
	v_and_b32_e32 v0, 15, v8
	v_lshlrev_b32_e32 v2, 1, v1
	v_lshl_or_b32 v145, s11, 6, v0
	v_lshl_or_b32 v0, v0, 6, v2
	v_lshlrev_b32_e32 v2, 2, v8
	s_lshl_b32 s11, s11, 13
	v_and_b32_e32 v2, 32, v2
	v_bitop3_b32 v3, v0, s11, v2 bitop3:0xde
	s_and_b32 s11, s7, 0x60
	v_or_b32_e32 v146, s11, v1
	v_lshlrev_b32_e32 v1, 14, v13
	v_and_b32_e32 v1, 0xffff8000, v1
	v_lshl_add_u32 v1, v12, 11, v1
	v_and_b32_e32 v4, 1, v13
	v_lshl_or_b32 v1, v4, 6, v1
	v_lshl_add_u32 v136, v14, 1, v1
	v_lshlrev_b32_e32 v1, 14, v9
	s_lshl_b32 s7, s11, 7
	v_and_b32_e32 v1, 0xffff8000, v1
	s_add_i32 s12, s8, 0x10800
	s_add_i32 s14, s8, 0x14800
	s_add_i32 s15, s8, 0x18800
	s_add_i32 s17, s8, 0x1c800
	v_bitop3_b32 v0, v0, s7, v2 bitop3:0xde
	s_waitcnt vmcnt(6)
	v_lshl_add_u32 v1, v10, 11, v1
	v_and_b32_e32 v4, 1, v9
	v_or_b32_e32 v2, 0x400, v0
	s_cmpk_lt_u32 s6, 0x100
	v_lshl_or_b32 v1, v4, 6, v1
	s_cselect_b64 s[6:7], -1, 0
	v_mov_b32_e32 v137, v133
	v_lshl_add_u32 v138, v11, 1, v1
	v_mov_b32_e32 v139, v133
	s_mov_b32 s54, 0
	v_add_u32_e32 v147, s10, v0
	v_add_u32_e32 v148, s10, v2
	v_add_u32_e32 v149, s12, v0
	v_add_u32_e32 v150, s12, v2
	v_add_u32_e32 v151, s9, v0
	v_add_u32_e32 v152, s9, v2
	v_add_u32_e32 v153, s14, v0
	v_add_u32_e32 v154, s14, v2
	v_add_u32_e32 v155, s8, v3
	v_add_u32_e32 v156, s13, v0
	v_add_u32_e32 v157, s13, v2
	v_add_u32_e32 v158, s15, v0
	v_add_u32_e32 v159, s15, v2
	v_add_u32_e32 v160, s16, v0
	v_add_u32_e32 v161, s16, v2
	v_add_u32_e32 v162, s17, v0
	v_add_u32_e32 v163, s17, v2
	s_mov_b32 s55, 0x40000
	s_mov_b64 s[8:9], 0x48000
	s_mov_b32 s58, 0x48000
	s_mov_b64 s[10:11], 0x50000
	s_mov_b32 s59, 0x50000
	s_mov_b64 s[12:13], 0x58000
	s_mov_b32 s60, 0x58000
	s_mov_b64 s[18:19], s[26:27]
	s_mov_b64 s[16:17], s[24:25]
	s_barrier
	s_branch .LBB0_318

; #define PG8_STAGE(bufoff, gbase, voff) do { _Pragma("unroll") for (int _i = 0; _i < 2; ++_i) \
;         __builtin_amdgcn_global_load_lds((const unsigned*)((const char*)(gbase) + (voff)[_i]), (LAS unsigned*)(lds + (bufoff) + ldsw + _i * 8192), 16, 0, 0); } while (0)
; #define PG8_WAIT_V(n) asm volatile("s_waitcnt vmcnt(" #n ")" ::: "memory")
; #define PG8_BAR __builtin_amdgcn_s_barrier()
; template <class Epi, class Sched, bool ALIGN_EPI = false, bool SP2 = false, bool FP8 = false  ,
;           bool GATHER = false  >
; __device__ __forceinline__ void gemm_phase(LAS unsigned char* lds, const Dims g, const Sched& S, const Epi& E, int tid_in) {
;     ...
;     const unsigned ldsw = (unsigned)wid * 1024u;
;     const int aoff0 = lds_byte(wr * 64 + fr, fq * 8), aoff1 = aoff0 + 1024;
;     const int boff0 = lds_byte(wc * 32 + fr, fq * 8), boff1 = boff0 + 1024;
;     ...
;         PG8_STAGE(PG8_SB(0, 0), cB, voffB); PG8_STAGE(PG8_SB(0, 1), cB + hstepB, voffB); PG8_STAGE_A(PG8_SA(0, 0), cA, 0, 0); PG8_STAGE_A(PG8_SA(0, 1), cA, 1, 0);
;         if (wr == 1) PG8_BAR;
;         PG8_WAIT_V(2); PG8_BAR;
;         PG8_STAGE(PG8_SB(1, 0), cB + kstep, voffB); PG8_STAGE_A(PG8_SA(1, 0), cA + kstep, 0, 0); PG8_STAGE(PG8_SB(1, 1), cB + hstepB + kstep, voffB);
;         PG8_WAIT_V(6); PG8_BAR;
.LBB0_399:
	s_add_u32 s6, s8, 0x3ce00000
	v_lshrrev_b32_e32 v15, 1, v12
	s_addc_u32 s7, s9, 0
	v_and_b32_e32 v16, 24, v15
	s_add_u32 s8, s8, 0x84740000
	v_and_b32_e32 v152, 15, v12
	v_lshlrev_b32_e32 v17, 1, v16
	v_lshlrev_b32_e32 v12, 2, v12
	s_addc_u32 s9, s9, 0
	s_add_i32 s61, s12, 0x18000
	s_lshl_b32 s70, s0, 6
	v_lshl_or_b32 v17, v152, 6, v17
	s_lshl_b32 s0, s0, 13
	v_and_b32_e32 v12, 32, v12
	v_bitop3_b32 v18, v17, s0, v12 bitop3:0xde
	s_lshl_b32 s0, s3, 5
	s_add_i32 s71, s61, s1
	s_and_b32 s0, s0, 0x60
	v_lshl_add_u64 v[6:7], v[6:7], 0, s[40:41]
	s_mov_b32 m0, s71
	s_add_i32 s72, s71, 0x2000
	s_add_i32 s62, s12, 0x1c000
	s_add_i32 s63, s12, 0x10800
	s_add_i32 s66, s12, 0x14800
	s_add_i32 s67, s12, 0x18800
	s_add_i32 s68, s12, 0x1c800
	s_ashr_i32 s69, s28, 31
	s_lshl_b32 s3, s0, 7
	global_load_lds_dwordx4 v[6:7], off
	v_lshl_add_u64 v[4:5], v[4:5], 0, s[40:41]
	s_mov_b32 m0, s72
	s_add_i32 s73, s57, 0x8000
	s_add_i32 s74, s57, 0xa000
	global_load_lds_dwordx4 v[4:5], off
	v_lshl_add_u64 v[0:1], v[0:1], 0, s[40:41]
	s_mov_b32 m0, s73
	s_add_u32 s14, s24, 0x20080
	global_load_lds_dwordx4 v[0:1], off
	v_lshl_add_u64 v[0:1], v[2:3], 0, s[40:41]
	s_mov_b32 m0, s74
	s_addc_u32 s15, s25, 0
	s_add_i32 s75, s62, s1
	global_load_lds_dwordx4 v[0:1], off
	v_lshl_add_u64 v[0:1], s[14:15], 0, v[132:133]
	s_mov_b32 m0, s75
	s_add_i32 s76, s75, 0x2000
	global_load_lds_dwordx4 v[0:1], off
	v_lshl_add_u64 v[0:1], s[14:15], 0, v[136:137]
	s_mov_b32 m0, s76
	v_and_b32_e32 v138, 8, v15
	global_load_lds_dwordx4 v[0:1], off
	s_waitcnt vmcnt(8)
	s_barrier
	v_lshlrev_b32_e32 v0, 5, v152
	v_mov_b32_e32 v1, v128
	v_lshl_add_u64 v[0:1], s[8:9], 0, v[0:1]
	v_lshlrev_b32_e32 v2, 1, v138
	v_mov_b32_e32 v3, v128
	v_lshl_add_u64 v[140:141], v[0:1], 0, v[2:3]
	v_lshlrev_b32_e32 v0, 13, v8
	v_and_b32_e32 v0, 0xffffc000, v0
	v_lshl_add_u32 v0, v9, 10, v0
	v_and_b32_e32 v1, 1, v8
	v_lshl_or_b32 v0, v1, 6, v0
	v_lshl_add_u32 v142, v10, 1, v0
	v_lshlrev_b32_e32 v0, 13, v11
	v_and_b32_e32 v0, 0xffffc000, v0
	s_waitcnt vmcnt(6)
	v_lshl_add_u32 v0, v13, 10, v0
	v_and_b32_e32 v1, 1, v11
	v_bitop3_b32 v153, v17, s3, v12 bitop3:0xde
	v_or_b32_e32 v155, s0, v16
	s_cmpk_lt_u32 s10, 0x100
	v_lshl_or_b32 v0, v1, 6, v0
	v_or_b32_e32 v154, 0x400, v153
	v_or_b32_e32 v156, 0x3fff400, v155
	s_cselect_b64 s[10:11], -1, 0
	v_mov_b32_e32 v143, v128
	v_lshl_add_u32 v144, v14, 1, v0
	v_mov_b32_e32 v145, v128
	s_mov_b32 s77, 0
	v_add_u32_e32 v157, s12, v18
	s_mov_b64 s[16:17], s[20:21]
	s_mov_b64 s[18:19], s[24:25]
	s_movk_i32 s42, 0xfe
	s_movk_i32 s43, 0x1000
	s_barrier
	s_branch .LBB0_402

; #define PG8_STAGE(bufoff, gbase, voff) do { _Pragma("unroll") for (int _i = 0; _i < 2; ++_i) \
;         __builtin_amdgcn_global_load_lds((const unsigned*)((const char*)(gbase) + (voff)[_i]), (LAS unsigned*)(lds + (bufoff) + ldsw + _i * 8192), 16, 0, 0); } while (0)
; #define PG8_WAIT_V(n) asm volatile("s_waitcnt vmcnt(" #n ")" ::: "memory")
; #define PG8_BAR __builtin_amdgcn_s_barrier()
; template <class Epi, class Sched, bool ALIGN_EPI = false, bool SP2 = false, bool FP8 = false  ,
;           bool GATHER = false  >
; __device__ __forceinline__ void gemm_phase(LAS unsigned char* lds, const Dims g, const Sched& S, const Epi& E, int tid_in) {
;     ...
;     const unsigned ldsw = (unsigned)wid * 1024u;
;     const int aoff0 = lds_byte(wr * 64 + fr, fq * 8), aoff1 = aoff0 + 1024;
;     const int boff0 = lds_byte(wc * 32 + fr, fq * 8), boff1 = boff0 + 1024;
;     ...
;         PG8_STAGE(PG8_SB(0, 0), cB, voffB); PG8_STAGE(PG8_SB(0, 1), cB + hstepB, voffB); PG8_STAGE_A(PG8_SA(0, 0), cA, 0, 0); PG8_STAGE_A(PG8_SA(0, 1), cA, 1, 0);
;         if (wr == 1) PG8_BAR;
;         PG8_WAIT_V(2); PG8_BAR;
;         PG8_STAGE(PG8_SB(1, 0), cB + kstep, voffB); PG8_STAGE_A(PG8_SA(1, 0), cA + kstep, 0, 0); PG8_STAGE(PG8_SB(1, 1), cB + hstepB + kstep, voffB);
;         PG8_WAIT_V(6); PG8_BAR;
.LBB0_576:
	v_lshrrev_b32_e32 v16, 1, v14
	v_and_b32_e32 v16, 24, v16
	v_and_b32_e32 v15, 15, v14
	v_lshlrev_b32_e32 v17, 1, v16
	v_lshlrev_b32_e32 v14, 2, v14
	v_lshl_or_b32 v79, s19, 6, v15
	v_lshl_or_b32 v15, v15, 6, v17
	s_lshl_b32 s13, s19, 13
	v_and_b32_e32 v14, 32, v14
	v_bitop3_b32 v17, v15, s13, v14 bitop3:0xde
	s_lshl_b32 s13, s18, 5
	s_and_b32 s13, s13, 0x60
	s_lshl_b32 s18, s13, 7
	s_add_i32 s62, s42, 0x18000
	v_bitop3_b32 v80, v15, s18, v14 bitop3:0xde
	s_add_u32 s18, s30, 0x20080
	s_addc_u32 s19, s31, 0
	s_add_i32 s46, s62, s17
	v_lshl_add_u64 v[6:7], v[6:7], 0, s[40:41]
	s_mov_b32 m0, s46
	s_add_i32 s67, s46, 0x2000
	global_load_lds_dwordx4 v[6:7], off
	v_lshl_add_u64 v[4:5], v[4:5], 0, s[40:41]
	s_mov_b32 m0, s67
	s_add_i32 s68, s58, 0x8000
	s_add_i32 s70, s42, 0x1c000
	global_load_lds_dwordx4 v[4:5], off
	v_lshl_add_u64 v[0:1], v[0:1], 0, s[40:41]
	s_mov_b32 m0, s68
	s_add_i32 s69, s58, 0xa000
	global_load_lds_dwordx4 v[0:1], off
	v_lshl_add_u64 v[0:1], v[2:3], 0, s[40:41]
	s_mov_b32 m0, s69
	s_add_i32 s70, s70, s17
	global_load_lds_dwordx4 v[0:1], off
	v_lshl_add_u64 v[0:1], s[18:19], 0, v[68:69]
	s_mov_b32 m0, s70
	s_add_i32 s71, s70, 0x2000
	global_load_lds_dwordx4 v[0:1], off
	v_lshl_add_u64 v[0:1], s[18:19], 0, v[64:65]
	s_mov_b32 m0, s71
	v_mul_lo_u32 v2, v11, s96
	global_load_lds_dwordx4 v[0:1], off
	s_waitcnt vmcnt(8)
	s_barrier
	v_or_b32_e32 v0, s13, v16
	v_lshrrev_b32_e32 v1, 1, v12
	s_movk_i32 s13, 0x5000
	v_mad_u64_u32 v[2:3], s[18:19], v1, s13, v[2:3]
	v_and_b32_e32 v1, 1, v12
	v_lshl_or_b32 v1, v1, 6, v2
	v_lshl_add_u32 v72, v13, 1, v1
	v_lshrrev_b32_e32 v1, 1, v8
	v_mul_lo_u32 v2, v9, s96
	s_add_i32 s63, s42, 0x10800
	s_add_i32 s66, s42, 0x18800
	s_waitcnt vmcnt(6)
	v_mad_u64_u32 v[2:3], s[18:19], v1, s13, v[2:3]
	v_and_b32_e32 v1, 1, v8
	s_cmpk_lt_u32 s16, 0x100
	v_lshl_or_b32 v1, v1, 6, v2
	v_or_b32_e32 v81, 0x400, v80
	s_cselect_b64 s[16:17], -1, 0
	v_mov_b32_e32 v73, v128
	v_lshl_add_u32 v74, v10, 1, v1
	v_mov_b32_e32 v75, v128
	s_mov_b32 s72, 0
	v_add_u32_e32 v82, s42, v17
	v_lshlrev_b32_e32 v76, 2, v0
	s_mov_b64 s[24:25], s[30:31]
	s_mov_b64 s[20:21], s[28:29]
	s_barrier
	s_branch .LBB0_579

; #define PG8_STAGE(bufoff, gbase, voff) do { _Pragma("unroll") for (int _i = 0; _i < 2; ++_i) \
;         __builtin_amdgcn_global_load_lds((const unsigned*)((const char*)(gbase) + (voff)[_i]), (LAS unsigned*)(lds + (bufoff) + ldsw + _i * 8192), 16, 0, 0); } while (0)
; #define PG8_WAIT_V(n) asm volatile("s_waitcnt vmcnt(" #n ")" ::: "memory")
; #define PG8_BAR __builtin_amdgcn_s_barrier()
; template <class Epi, class Sched, bool ALIGN_EPI = false, bool SP2 = false, bool FP8 = false  ,
;           bool GATHER = false  >
; __device__ __forceinline__ void gemm_phase(LAS unsigned char* lds, const Dims g, const Sched& S, const Epi& E, int tid_in) {
;     ...
;     const unsigned ldsw = (unsigned)wid * 1024u;
;     const int aoff0 = lds_byte(wr * 64 + fr, fq * 8), aoff1 = aoff0 + 1024;
;     const int boff0 = lds_byte(wc * 32 + fr, fq * 8), boff1 = boff0 + 1024;
;     ...
;         PG8_STAGE(PG8_SB(0, 0), cB, voffB); PG8_STAGE(PG8_SB(0, 1), cB + hstepB, voffB); PG8_STAGE_A(PG8_SA(0, 0), cA, 0, 0); PG8_STAGE_A(PG8_SA(0, 1), cA, 1, 0);
;         if (wr == 1) PG8_BAR;
;         PG8_WAIT_V(2); PG8_BAR;
;         PG8_STAGE(PG8_SB(1, 0), cB + kstep, voffB); PG8_STAGE_A(PG8_SA(1, 0), cA + kstep, 0, 0); PG8_STAGE(PG8_SB(1, 1), cB + hstepB + kstep, voffB);
;         PG8_WAIT_V(6); PG8_BAR;
.LBB0_670:
	v_lshrrev_b32_e32 v16, 1, v14
	v_and_b32_e32 v17, 24, v16
	s_lshl_b32 s4, s4, 5
	v_and_b32_e32 v15, 15, v14
	v_lshlrev_b32_e32 v18, 1, v17
	v_lshlrev_b32_e32 v14, 2, v14
	s_and_b32 s10, s4, 0x60
	v_lshl_or_b32 v139, s5, 6, v15
	v_lshl_or_b32 v15, v15, 6, v18
	s_lshl_b32 s5, s5, 13
	v_and_b32_e32 v14, 32, v14
	s_lshl_b32 s4, s10, 7
	v_bitop3_b32 v141, v15, s4, v14 bitop3:0xde
	s_add_u32 s4, s29, 0x53200000
	v_bitop3_b32 v18, v15, s5, v14 bitop3:0xde
	s_addc_u32 s5, s28, 0
	s_add_i32 s61, s26, 0x18000
	s_add_u32 s8, s20, 0x28080
	s_addc_u32 s9, s21, 0
	s_add_i32 s72, s61, s7
	v_lshl_add_u64 v[6:7], v[6:7], 0, s[40:41]
	s_mov_b32 m0, s72
	s_add_i32 s73, s72, 0x2000
	global_load_lds_dwordx4 v[6:7], off
	v_lshl_add_u64 v[4:5], v[4:5], 0, s[40:41]
	s_mov_b32 m0, s73
	s_add_i32 s74, s57, 0x8000
	s_add_i32 s62, s26, 0x1c000
	global_load_lds_dwordx4 v[4:5], off
	v_lshl_add_u64 v[0:1], v[0:1], 0, s[40:41]
	s_mov_b32 m0, s74
	s_add_i32 s75, s57, 0xa000
	global_load_lds_dwordx4 v[0:1], off
	v_lshl_add_u64 v[0:1], v[2:3], 0, s[40:41]
	s_mov_b32 m0, s75
	s_add_i32 s76, s62, s7
	global_load_lds_dwordx4 v[0:1], off
	v_lshl_add_u64 v[0:1], s[8:9], 0, v[134:135]
	s_mov_b32 m0, s76
	s_add_i32 s77, s76, 0x2000
	global_load_lds_dwordx4 v[0:1], off
	v_lshl_add_u64 v[0:1], s[8:9], 0, v[130:131]
	s_mov_b32 m0, s77
	v_or_b32_e32 v145, s10, v17
	global_load_lds_dwordx4 v[0:1], off
	s_waitcnt vmcnt(8)
	s_barrier
	v_lshlrev_b32_e32 v1, 5, v139
	v_and_b32_e32 v138, 0x19e0, v1
	v_lshrrev_b32_e32 v1, 1, v12
	v_mul_lo_u32 v2, v11, s96
	s_movk_i32 s10, 0x5000
	v_mad_u64_u32 v[2:3], s[8:9], v1, s10, v[2:3]
	v_and_b32_e32 v1, 1, v12
	v_lshl_or_b32 v1, v1, 6, v2
	v_lshl_add_u32 v146, v13, 1, v1
	v_lshrrev_b32_e32 v1, 1, v8
	v_mul_lo_u32 v2, v9, s96
	s_add_i32 s63, s26, 0x10800
	s_add_i32 s66, s26, 0x14800
	s_add_i32 s67, s26, 0x18800
	s_add_i32 s69, s26, 0x1c800
	s_waitcnt vmcnt(6)
	v_mad_u64_u32 v[2:3], s[8:9], v1, s10, v[2:3]
	v_and_b32_e32 v1, 1, v8
	s_cmpk_lt_u32 s6, 0x100
	v_and_b32_e32 v0, 8, v16
	v_lshl_or_b32 v1, v1, 6, v2
	v_or_b32_e32 v143, 0x400, v141
	s_cselect_b64 s[6:7], -1, 0
	v_or_b32_e32 v140, 0x200, v138
	v_or_b32_e32 v142, 0x400, v138
	v_or_b32_e32 v144, 0x600, v138
	v_mov_b32_e32 v147, v128
	v_lshl_add_u32 v148, v10, 1, v1
	v_mov_b32_e32 v149, v128
	s_mov_b32 s78, 0
	v_add_u32_e32 v157, s26, v18
	v_lshlrev_b32_e32 v150, 1, v0
	s_mov_b64 s[12:13], s[20:21]
	s_mov_b64 s[10:11], s[18:19]
	s_barrier
	s_branch .LBB0_673

; #define LAS __attribute__((address_space(3)))
; #define LDS_WAIT() asm volatile("s_waitcnt lgkmcnt(0)" ::: "memory")
; #define SHI(v, s) bperm_((s), (v))
; __device__ __forceinline__ bool dsa2_sampled(LAS unsigned char* wl, const unsigned (&kk)[128], int nreg, int n, int lane) {
;     ...
;     if (A > 256 || A + C < 256) return false;
;     LDS_WAIT();
;     unsigned need = 256u - (unsigned)A; const int nit = (C + 63) >> 6;
;     if (need > 0u) { unsigned long long prefix = 0ull; int shf = 45;
; #pragma unroll 1
;         for (int lev = 0; lev < 6; ++lev) { const int w = lev < 5 ? 8 : 5; const int sh = shf - w;
;             { unsigned zq_ = 0u; asm volatile("" : "+v"(zq_)); *(LAS v4u*)(h2 + 4 * lane) = (v4u){zq_, zq_, zq_, zq_}; }
;             LDS_WAIT();
;             for (int it = 0; it < nit; ++it) { const int i = it * 64 + lane; if (i < C) { const unsigned long long c2 = PRIV[i]; if (lev == 0 || (c2 >> shf) == prefix) (void)__hip_atomic_fetch_add(&h2[(unsigned)(c2 >> sh) & ((1u << w) - 1u)], 1u, __ATOMIC_RELAXED, __HIP_MEMORY_SCOPE_WORKGROUP); } }
;             LDS_WAIT();
;             const v4u v = *(const LAS v4u*)(h2 + 4 * lane); const unsigned m4 = (v.x + v.y) + (v.z + v.w); const unsigned pr2_ = dpp_scan_add_u32(m4); const unsigned in2 = (unsigned)__builtin_amdgcn_readlane((int)pr2_, 63) - pr2_ + m4;
;             const unsigned ab = in2 - m4; const bool fnd = ab < need && need <= ab + m4;
;             unsigned a = ab; int bs = 0; bool dn = false; const unsigned h4[4] = {v.x, v.y, v.z, v.w};
; #pragma unroll
;             for (int i = 3; i >= 0; --i) { const bool hit = !dn && (need <= a + h4[i]); bs = hit ? i : bs; a = (dn || hit) ? a : a + h4[i]; dn = dn || hit; }
;             const int src = __builtin_ctzll(__ballot(fnd));
;             const unsigned bf = (unsigned)SHI(lane * 4 + bs, src); const unsigned aa = (unsigned)SHI((int)a, src); const unsigned hb = (unsigned)SHI((int)(bs == 3 ? h4[3] : bs == 2 ? h4[2] : bs == 1 ? h4[1] : h4[0]), src);
;             prefix = (prefix << w) | bf; need -= aa; shf = sh;
.LBB0_1247:
	s_cmpk_gt_u32 s20, 0x100
	s_cselect_b64 s[0:1], -1, 0
	s_add_i32 s2, s20, s21
	s_cmpk_lt_u32 s2, 0x100
	s_cselect_b64 s[2:3], -1, 0
	s_or_b64 s[0:1], s[0:1], s[2:3]
	s_andn2_b64 vcc, exec, s[0:1]
	s_mov_b64 s[0:1], -1
	s_cbranch_vccz .LBB0_1271
	s_waitcnt lgkmcnt(0)
	s_cmpk_eq_i32 s20, 0x100
	s_cbranch_scc1 .LBB0_1270
	s_add_i32 s0, s21, 63
	s_lshr_b32 s46, s0, 6
	s_sub_i32 s0, 0x100, s20
	v_lshlrev_b32_e32 v0, 3, v129
	s_cmp_lg_u32 s21, 0
	s_mov_b32 s84, s62
	v_lshlrev_b32_e32 v7, 2, v129
	s_mov_b32 s59, 0
	s_mov_b32 s62, 45
	s_mov_b64 s[12:13], 0
	s_cselect_b64 s[14:15], -1, 0
	v_mov_b32_e32 v8, s0
	v_mov_b64_e32 v[4:5], 0
	v_add_u32_e32 v9, v6, v0
	v_readfirstlane_b32 s0, v2
	v_readfirstlane_b32 s1, v168
	s_min_u32 s1, s1, s0
	s_lshr_b32 s1, s1, 3
	s_lshr_b32 s0, s0, 3
	s_cmp_lg_u32 s0, s1
	s_cbranch_scc1 .Lrdx_full
	s_mov_b32 s59, 1
	s_mov_b32 s62, 37
	v_mov_b32_e32 v4, s0
.Lrdx_full:
	s_branch .LBB0_1252
.LBB0_1250:
	s_or_b64 exec, exec, s[4:5]

; #define PG8_STAGE(bufoff, gbase, voff) do { _Pragma("unroll") for (int _i = 0; _i < 2; ++_i) \
;         __builtin_amdgcn_global_load_lds((const unsigned*)((const char*)(gbase) + (voff)[_i]), (LAS unsigned*)(lds + (bufoff) + ldsw + _i * 8192), 16, 0, 0); } while (0)
; #define PG8_WAIT_V(n) asm volatile("s_waitcnt vmcnt(" #n ")" ::: "memory")
; #define PG8_BAR __builtin_amdgcn_s_barrier()
; template <class Epi, class Sched, bool ALIGN_EPI = false, bool SP2 = false, bool FP8 = false  ,
;           bool GATHER = false  >
; __device__ __forceinline__ void gemm_phase(LAS unsigned char* lds, const Dims g, const Sched& S, const Epi& E, int tid_in) {
;     ...
;     const unsigned ldsw = (unsigned)wid * 1024u;
;     const int aoff0 = lds_byte(wr * 64 + fr, fq * 8), aoff1 = aoff0 + 1024;
;     const int boff0 = lds_byte(wc * 32 + fr, fq * 8), boff1 = boff0 + 1024;
;     ...
;         PG8_STAGE(PG8_SB(0, 0), cB, voffB); PG8_STAGE(PG8_SB(0, 1), cB + hstepB, voffB); PG8_STAGE_A(PG8_SA(0, 0), cA, 0, 0); PG8_STAGE_A(PG8_SA(0, 1), cA, 1, 0);
;         if (wr == 1) PG8_BAR;
;         PG8_WAIT_V(2); PG8_BAR;
;         PG8_STAGE(PG8_SB(1, 0), cB + kstep, voffB); PG8_STAGE_A(PG8_SA(1, 0), cA + kstep, 0, 0); PG8_STAGE(PG8_SB(1, 1), cB + hstepB + kstep, voffB);
;         PG8_WAIT_V(6); PG8_BAR;
.LBB0_2760:
	v_lshrrev_b32_e32 v16, 1, v14
	s_lshl_b64 s[12:13], s[22:23], 2
	v_and_b32_e32 v16, 24, v16
	s_add_u32 s6, s6, s12
	v_and_b32_e32 v15, 15, v14
	v_lshlrev_b32_e32 v17, 1, v16
	v_lshlrev_b32_e32 v14, 2, v14
	s_sext_i32_i8 s81, s0
	s_addc_u32 s7, s7, s13
	v_lshl_or_b32 v199, s11, 6, v15
	v_lshl_or_b32 v15, v15, 6, v17
	s_lshl_b32 s0, s11, 13
	v_and_b32_e32 v14, 32, v14
	v_bitop3_b32 v17, v15, s0, v14 bitop3:0xde
	s_lshl_b32 s0, s9, 5
	s_and_b32 s0, s0, 0x60
	s_lshl_b32 s9, s0, 7
	s_sub_i32 s22, s8, s29
	s_add_u32 s8, s57, 0x4f200800
	v_bitop3_b32 v200, v15, s9, v14 bitop3:0xde
	s_addc_u32 s9, s56, 0
	s_add_i32 s74, s34, s10
	v_lshl_add_u64 v[6:7], v[6:7], 0, s[40:41]
	s_mov_b32 m0, s74
	s_add_i32 s75, s74, 0x2000
	s_ashr_i32 s73, s22, 31
	global_load_lds_dwordx4 v[6:7], off
	v_lshl_add_u64 v[4:5], v[4:5], 0, s[40:41]
	s_mov_b32 m0, s75
	s_add_i32 s76, s69, 0x8000
	s_add_i32 s77, s69, 0xa000
	global_load_lds_dwordx4 v[4:5], off
	v_lshl_add_u64 v[0:1], v[0:1], 0, s[40:41]
	s_mov_b32 m0, s76
	s_add_u32 s12, s24, 0x20080
	global_load_lds_dwordx4 v[0:1], off
	v_lshl_add_u64 v[0:1], v[2:3], 0, s[40:41]
	s_mov_b32 m0, s77
	s_addc_u32 s13, s25, 0
	s_add_i32 s78, s35, s10
	global_load_lds_dwordx4 v[0:1], off
	v_lshl_add_u64 v[0:1], s[12:13], 0, v[178:179]
	s_mov_b32 m0, s78
	s_add_i32 s79, s78, 0x2000
	global_load_lds_dwordx4 v[0:1], off
	v_lshl_add_u64 v[0:1], s[12:13], 0, v[174:175]
	s_mov_b32 m0, s79
	s_cmpk_lt_u32 s1, 0x100
	global_load_lds_dwordx4 v[0:1], off
	s_waitcnt vmcnt(8)
	s_barrier
	v_lshlrev_b32_e32 v0, 13, v12
	v_and_b32_e32 v0, 0xffffc000, v0
	v_lshl_add_u32 v0, v11, 10, v0
	v_and_b32_e32 v1, 1, v12
	v_lshl_or_b32 v0, v1, 6, v0
	v_lshl_add_u32 v182, v13, 1, v0
	v_lshlrev_b32_e32 v0, 13, v8
	v_and_b32_e32 v0, 0xffffc000, v0
	s_waitcnt vmcnt(6)
	v_lshl_add_u32 v0, v9, 10, v0
	v_and_b32_e32 v1, 1, v8
	v_lshl_or_b32 v0, v1, 6, v0
	v_or_b32_e32 v201, 0x400, v200
	s_cselect_b64 s[10:11], -1, 0
	v_or_b32_e32 v202, s0, v16
	v_mov_b32_e32 v183, v128
	v_lshl_add_u32 v184, v10, 1, v0
	v_mov_b32_e32 v185, v128
	s_mov_b32 s80, 0
	v_add_u32_e32 v203, s51, v17
	s_mov_b64 s[16:17], s[20:21]
	s_mov_b64 s[18:19], s[24:25]
	s_barrier
	s_branch .LBB0_2763

; #define PG8_STAGE(bufoff, gbase, voff) do { _Pragma("unroll") for (int _i = 0; _i < 2; ++_i) \
;         __builtin_amdgcn_global_load_lds((const unsigned*)((const char*)(gbase) + (voff)[_i]), (LAS unsigned*)(lds + (bufoff) + ldsw + _i * 8192), 16, 0, 0); } while (0)
; #define PG8_WAIT_V(n) asm volatile("s_waitcnt vmcnt(" #n ")" ::: "memory")
; #define PG8_BAR __builtin_amdgcn_s_barrier()
; template <class Epi, class Sched, bool ALIGN_EPI = false, bool SP2 = false, bool FP8 = false  ,
;           bool GATHER = false  >
; __device__ __forceinline__ void gemm_phase(LAS unsigned char* lds, const Dims g, const Sched& S, const Epi& E, int tid_in) {
;     ...
;     const unsigned ldsw = (unsigned)wid * 1024u;
;     const int aoff0 = lds_byte(wr * 64 + fr, fq * 8), aoff1 = aoff0 + 1024;
;     const int boff0 = lds_byte(wc * 32 + fr, fq * 8), boff1 = boff0 + 1024;
;     ...
;         PG8_STAGE(PG8_SB(0, 0), cB, voffB); PG8_STAGE(PG8_SB(0, 1), cB + hstepB, voffB); PG8_STAGE_A(PG8_SA(0, 0), cA, 0, 0); PG8_STAGE_A(PG8_SA(0, 1), cA, 1, 0);
;         if (wr == 1) PG8_BAR;
;         PG8_WAIT_V(2); PG8_BAR;
;         PG8_STAGE(PG8_SB(1, 0), cB + kstep, voffB); PG8_STAGE_A(PG8_SA(1, 0), cA + kstep, 0, 0); PG8_STAGE(PG8_SB(1, 1), cB + hstepB + kstep, voffB);
;         PG8_WAIT_V(6); PG8_BAR;
.LBB0_2782:
	v_lshrrev_b32_e32 v16, 1, v14
	v_and_b32_e32 v16, 24, v16
	v_and_b32_e32 v15, 15, v14
	v_lshlrev_b32_e32 v17, 1, v16
	v_lshlrev_b32_e32 v14, 2, v14
	s_sext_i32_i8 s71, s2
	v_lshl_or_b32 v145, s6, 6, v15
	v_lshl_or_b32 v15, v15, 6, v17
	s_lshl_b32 s2, s6, 13
	v_and_b32_e32 v14, 32, v14
	v_bitop3_b32 v17, v15, s2, v14 bitop3:0xde
	s_lshl_b32 s2, s3, 5
	s_and_b32 s8, s2, 0x60
	s_lshl_b32 s2, s8, 7
	v_bitop3_b32 v146, v15, s2, v14 bitop3:0xde
	s_add_u32 s2, s57, 0x4f200000
	s_addc_u32 s3, s56, 0
	s_add_i32 s56, s34, s5
	v_lshl_add_u64 v[6:7], v[6:7], 0, s[40:41]
	s_mov_b32 m0, s56
	s_add_i32 s57, s56, 0x2000
	global_load_lds_dwordx4 v[6:7], off
	v_lshl_add_u64 v[4:5], v[4:5], 0, s[40:41]
	s_mov_b32 m0, s57
	s_add_i32 s66, s60, 0x8000
	s_add_i32 s67, s60, 0xa000
	global_load_lds_dwordx4 v[4:5], off
	v_lshl_add_u64 v[0:1], v[0:1], 0, s[40:41]
	s_mov_b32 m0, s66
	s_add_u32 s6, s18, 0x40080
	global_load_lds_dwordx4 v[0:1], off
	v_lshl_add_u64 v[0:1], v[2:3], 0, s[40:41]
	s_mov_b32 m0, s67
	s_addc_u32 s7, s19, 0
	s_add_i32 s68, s35, s5
	global_load_lds_dwordx4 v[0:1], off
	v_lshl_add_u64 v[0:1], s[6:7], 0, v[134:135]
	s_mov_b32 m0, s68
	s_add_i32 s69, s68, 0x2000
	global_load_lds_dwordx4 v[0:1], off
	v_lshl_add_u64 v[0:1], s[6:7], 0, v[130:131]
	s_mov_b32 m0, s69
	s_cmpk_lt_u32 s4, 0x100
	global_load_lds_dwordx4 v[0:1], off
	s_waitcnt vmcnt(8)
	s_barrier
	v_lshlrev_b32_e32 v0, 14, v12
	v_and_b32_e32 v0, 0xffff8000, v0
	v_lshl_add_u32 v0, v11, 11, v0
	v_and_b32_e32 v1, 1, v12
	v_lshl_or_b32 v0, v1, 6, v0
	v_lshl_add_u32 v138, v13, 1, v0
	v_lshlrev_b32_e32 v0, 14, v8
	v_and_b32_e32 v0, 0xffff8000, v0
	s_waitcnt vmcnt(6)
	v_lshl_add_u32 v0, v9, 11, v0
	v_and_b32_e32 v1, 1, v8
	v_lshl_or_b32 v0, v1, 6, v0
	v_or_b32_e32 v147, 0x400, v146
	s_cselect_b64 s[4:5], -1, 0
	v_or_b32_e32 v148, s8, v16
	v_mov_b32_e32 v139, v128
	v_lshl_add_u32 v140, v10, 1, v0
	v_mov_b32_e32 v141, v128
	s_mov_b32 s70, 0
	v_add_u32_e32 v149, s51, v17
	s_mov_b64 s[10:11], s[16:17]
	s_mov_b64 s[12:13], s[18:19]
	s_barrier
	s_branch .LBB0_2785

; #define PG8_STAGE(bufoff, gbase, voff) do { _Pragma("unroll") for (int _i = 0; _i < 2; ++_i) \
;         __builtin_amdgcn_global_load_lds((const unsigned*)((const char*)(gbase) + (voff)[_i]), (LAS unsigned*)(lds + (bufoff) + ldsw + _i * 8192), 16, 0, 0); } while (0)
; #define PG8_WAIT_V(n) asm volatile("s_waitcnt vmcnt(" #n ")" ::: "memory")
; #define PG8_BAR __builtin_amdgcn_s_barrier()
; template <class Epi, class Sched, bool ALIGN_EPI = false, bool SP2 = false, bool FP8 = false  ,
;           bool GATHER = false  >
; __device__ __forceinline__ void gemm_phase(LAS unsigned char* lds, const Dims g, const Sched& S, const Epi& E, int tid_in) {
;     ...
;     const unsigned ldsw = (unsigned)wid * 1024u;
;     const int aoff0 = lds_byte(wr * 64 + fr, fq * 8), aoff1 = aoff0 + 1024;
;     const int boff0 = lds_byte(wc * 32 + fr, fq * 8), boff1 = boff0 + 1024;
;     ...
;         PG8_STAGE(PG8_SB(0, 0), cB, voffB); PG8_STAGE(PG8_SB(0, 1), cB + hstepB, voffB); PG8_STAGE_A(PG8_SA(0, 0), cA, 0, 0); PG8_STAGE_A(PG8_SA(0, 1), cA, 1, 0);
;         if (wr == 1) PG8_BAR;
;         PG8_WAIT_V(2); PG8_BAR;
;         PG8_STAGE(PG8_SB(1, 0), cB + kstep, voffB); PG8_STAGE_A(PG8_SA(1, 0), cA + kstep, 0, 0); PG8_STAGE(PG8_SB(1, 1), cB + hstepB + kstep, voffB);
;         PG8_WAIT_V(6); PG8_BAR;
.LBB0_2867:
	s_add_u32 s6, s11, 0x58200000
	v_lshrrev_b32_e32 v16, 1, v12
	s_addc_u32 s7, s9, 0
	v_and_b32_e32 v16, 24, v16
	s_add_u32 s57, s11, 0x3ce02000
	v_and_b32_e32 v15, 15, v12
	v_lshlrev_b32_e32 v17, 1, v16
	v_lshlrev_b32_e32 v12, 2, v12
	s_addc_u32 s58, s9, 0
	s_add_i32 s59, s10, 0x18000
	v_lshl_or_b32 v232, s0, 6, v15
	v_lshl_or_b32 v15, v15, 6, v17
	s_lshl_b32 s0, s0, 13
	v_and_b32_e32 v12, 32, v12
	v_bitop3_b32 v17, v15, s0, v12 bitop3:0xde
	s_lshl_b32 s0, s3, 5
	s_add_i32 s67, s59, s1
	s_and_b32 s0, s0, 0x60
	v_lshl_add_u64 v[6:7], v[6:7], 0, s[40:41]
	s_mov_b32 m0, s67
	s_add_i32 s68, s67, 0x2000
	s_add_i32 s60, s10, 0x1c000
	s_add_i32 s61, s10, 0x10800
	s_add_i32 s62, s10, 0x14800
	s_add_i32 s63, s10, 0x18800
	s_add_i32 s66, s10, 0x1c800
	s_lshl_b32 s3, s0, 7
	global_load_lds_dwordx4 v[6:7], off
	v_lshl_add_u64 v[4:5], v[4:5], 0, s[40:41]
	s_mov_b32 m0, s68
	s_add_i32 s69, s49, 0x8000
	s_add_i32 s70, s49, 0xa000
	global_load_lds_dwordx4 v[4:5], off
	v_lshl_add_u64 v[0:1], v[0:1], 0, s[40:41]
	s_mov_b32 m0, s69
	s_add_u32 s12, s18, 0x20080
	global_load_lds_dwordx4 v[0:1], off
	v_lshl_add_u64 v[0:1], v[2:3], 0, s[40:41]
	s_mov_b32 m0, s70
	s_addc_u32 s13, s19, 0
	s_add_i32 s71, s60, s1
	global_load_lds_dwordx4 v[0:1], off
	v_lshl_add_u64 v[0:1], s[12:13], 0, v[200:201]
	s_mov_b32 m0, s71
	s_add_i32 s72, s71, 0x2000
	global_load_lds_dwordx4 v[0:1], off
	v_lshl_add_u64 v[0:1], s[12:13], 0, v[204:205]
	s_mov_b32 m0, s72
	v_bitop3_b32 v233, v15, s3, v12 bitop3:0xde
	global_load_lds_dwordx4 v[0:1], off
	s_waitcnt vmcnt(8)
	s_barrier
	v_lshlrev_b32_e32 v0, 15, v8
	v_and_b32_e32 v0, 0xffff0000, v0
	v_lshl_add_u32 v0, v9, 12, v0
	v_and_b32_e32 v1, 1, v8
	v_lshl_or_b32 v0, v1, 6, v0
	v_lshl_add_u32 v206, v10, 1, v0
	v_lshlrev_b32_e32 v0, 15, v11
	v_and_b32_e32 v0, 0xffff0000, v0
	s_waitcnt vmcnt(6)
	v_lshl_add_u32 v0, v13, 12, v0
	v_and_b32_e32 v1, 1, v11
	s_cmpk_lt_u32 s8, 0x100
	v_lshl_or_b32 v0, v1, 6, v0
	v_or_b32_e32 v234, 0x400, v233
	s_cselect_b64 s[8:9], -1, 0
	v_or_b32_e32 v235, s0, v16
	v_mov_b32_e32 v207, v128
	v_lshl_add_u32 v208, v14, 1, v0
	v_mov_b32_e32 v209, v128
	s_mov_b32 s3, 0
	v_add_u32_e32 v236, s10, v17
	s_mov_b32 s73, 0
	s_mov_b64 s[12:13], s[16:17]
	s_mov_b64 s[14:15], s[18:19]
	s_barrier
	s_branch .LBB0_2870

; #define PG8_STAGE(bufoff, gbase, voff) do { _Pragma("unroll") for (int _i = 0; _i < 2; ++_i) \
;         __builtin_amdgcn_global_load_lds((const unsigned*)((const char*)(gbase) + (voff)[_i]), (LAS unsigned*)(lds + (bufoff) + ldsw + _i * 8192), 16, 0, 0); } while (0)
; #define PG8_WAIT_V(n) asm volatile("s_waitcnt vmcnt(" #n ")" ::: "memory")
; #define PG8_BAR __builtin_amdgcn_s_barrier()
; template <class Epi, class Sched, bool ALIGN_EPI = false, bool SP2 = false, bool FP8 = false  ,
;           bool GATHER = false  >
; __device__ __forceinline__ void gemm_phase(LAS unsigned char* lds, const Dims g, const Sched& S, const Epi& E, int tid_in) {
;     ...
;         PG8_STAGE(PG8_SB(0, 0), cB, voffB); PG8_STAGE(PG8_SB(0, 1), cB + hstepB, voffB); PG8_STAGE_A(PG8_SA(0, 0), cA, 0, 0); PG8_STAGE_A(PG8_SA(0, 1), cA, 1, 0);
;         if (wr == 1) PG8_BAR;
;         PG8_WAIT_V(2); PG8_BAR;
;         PG8_STAGE(PG8_SB(1, 0), cB + kstep, voffB); PG8_STAGE_A(PG8_SA(1, 0), cA + kstep, 0, 0); PG8_STAGE(PG8_SB(1, 1), cB + hstepB + kstep, voffB);
;         PG8_WAIT_V(6); PG8_BAR;
.LBB0_3265:
	v_lshrrev_b32_e32 v7, 1, v215
	v_and_b32_e32 v7, 24, v7
	s_lshl_b64 s[42:43], s[22:23], 2
	v_and_b32_e32 v6, 15, v215
	v_lshlrev_b32_e32 v8, 1, v7
	s_add_u32 s16, s16, s42
	v_lshl_or_b32 v253, s4, 6, v6
	v_lshl_or_b32 v6, v6, 6, v8
	v_lshlrev_b32_e32 v8, 2, v215
	s_addc_u32 s17, s17, s43
	s_lshl_b32 s4, s4, 13
	v_and_b32_e32 v9, 32, v8
	v_bitop3_b32 v10, v6, s4, v9 bitop3:0xde
	s_lshl_b32 s4, s18, 5
	s_and_b32 s4, s4, 0x60
	s_lshl_b32 s18, s4, 7
	v_bitop3_b32 v254, v6, s18, v9 bitop3:0xde
	s_add_u32 s18, s2, 0x6e640000
	s_addc_u32 s19, s3, 0
	s_add_i32 s22, s20, 0x18000
	v_mov_b32_e32 v223, v128
	s_add_i32 s89, s22, s5
	v_lshl_add_u64 v[2:3], v[0:1], 0, v[222:223]
	v_mov_b32_e32 v225, v128
	s_add_i32 s83, s20, 0x1c000
	s_add_i32 s84, s20, 0x10800
	s_add_i32 s85, s20, 0x14800
	s_add_i32 s86, s20, 0x18800
	s_add_i32 s87, s20, 0x1c800
	s_ashr_i32 s88, s24, 31
	s_add_i32 s90, s89, 0x2000
	v_lshl_add_u64 v[4:5], v[0:1], 0, v[224:225]
	v_lshl_add_u64 v[2:3], v[2:3], 0, s[40:41]
	s_mov_b32 m0, s89
	s_add_u32 s68, s2, 0x62200080
	v_mov_b32_e32 v233, v128
	global_load_lds_dwordx4 v[2:3], off
	v_lshl_add_u64 v[2:3], v[4:5], 0, s[40:41]
	s_mov_b32 m0, s90
	s_addc_u32 s69, s3, 0
	s_add_i32 s91, s79, 0x8000
	v_mov_b32_e32 v235, v128
	global_load_lds_dwordx4 v[2:3], off
	v_lshl_add_u64 v[2:3], s[68:69], 0, v[232:233]
	s_mov_b32 m0, s91
	s_add_i32 s92, s79, 0xa000
	global_load_lds_dwordx4 v[2:3], off
	v_lshl_add_u64 v[2:3], s[68:69], 0, v[234:235]
	s_mov_b32 m0, s92
	s_mov_b64 s[2:3], 0x20080
	global_load_lds_dwordx4 v[2:3], off
	v_lshl_add_u64 v[2:3], v[0:1], 0, s[2:3]
	s_add_i32 s93, s83, s5
	v_lshl_add_u64 v[4:5], v[2:3], 0, v[222:223]
	s_mov_b32 m0, s93
	s_add_i32 s94, s93, 0x2000
	global_load_lds_dwordx4 v[4:5], off
	v_lshl_add_u64 v[2:3], v[2:3], 0, v[224:225]
	s_mov_b32 m0, s94
	s_cmpk_lt_u32 s6, 0x100
	global_load_lds_dwordx4 v[2:3], off
	s_waitcnt vmcnt(8)
	s_barrier
	s_waitcnt vmcnt(6)
	v_or_b32_e32 v216, 0x400, v254
	v_add_u32_e32 v217, s7, v8
	s_cselect_b64 s[70:71], -1, 0
	v_ashrrev_i32_e32 v221, 31, v220
	v_or_b32_e32 v233, s4, v7
	s_mov_b32 s95, 0
	v_add_u32_e32 v235, s20, v10
	v_mov_b64_e32 v[228:229], v[0:1]
	s_barrier
	s_branch .LBB0_3268

; #define PG8_STAGE(bufoff, gbase, voff) do { _Pragma("unroll") for (int _i = 0; _i < 2; ++_i) \
;         __builtin_amdgcn_global_load_lds((const unsigned*)((const char*)(gbase) + (voff)[_i]), (LAS unsigned*)(lds + (bufoff) + ldsw + _i * 8192), 16, 0, 0); } while (0)
; #define PG8_WAIT_V(n) asm volatile("s_waitcnt vmcnt(" #n ")" ::: "memory")
; #define PG8_BAR __builtin_amdgcn_s_barrier()
; template <class Epi, class Sched, bool ALIGN_EPI = false, bool SP2 = false, bool FP8 = false  ,
;           bool GATHER = false  >
; __device__ __forceinline__ void gemm_phase(LAS unsigned char* lds, const Dims g, const Sched& S, const Epi& E, int tid_in) {
;     ...
;     const unsigned ldsw = (unsigned)wid * 1024u;
;     const int aoff0 = lds_byte(wr * 64 + fr, fq * 8), aoff1 = aoff0 + 1024;
;     const int boff0 = lds_byte(wc * 32 + fr, fq * 8), boff1 = boff0 + 1024;
;     ...
;         PG8_STAGE(PG8_SB(0, 0), cB, voffB); PG8_STAGE(PG8_SB(0, 1), cB + hstepB, voffB); PG8_STAGE_A(PG8_SA(0, 0), cA, 0, 0); PG8_STAGE_A(PG8_SA(0, 1), cA, 1, 0);
;         if (wr == 1) PG8_BAR;
;         PG8_WAIT_V(2); PG8_BAR;
;         PG8_STAGE(PG8_SB(1, 0), cB + kstep, voffB); PG8_STAGE_A(PG8_SA(1, 0), cA + kstep, 0, 0); PG8_STAGE(PG8_SB(1, 1), cB + hstepB + kstep, voffB);
;         PG8_WAIT_V(6); PG8_BAR;
.LBB0_3418:
	s_lshl_b64 s[12:13], s[22:23], 2
	s_add_u32 s6, s6, s12
	v_lshrrev_b32_e32 v18, 1, v12
	s_addc_u32 s7, s7, s13
	v_and_b32_e32 v18, 24, v18
	s_lshl_b32 s8, s8, 5
	v_and_b32_e32 v13, 15, v12
	v_lshlrev_b32_e32 v19, 1, v18
	v_lshlrev_b32_e32 v12, 2, v12
	s_and_b32 s15, s8, 0x60
	v_lshl_or_b32 v165, s9, 6, v13
	v_lshl_or_b32 v13, v13, 6, v19
	s_lshl_b32 s9, s9, 13
	v_and_b32_e32 v12, 32, v12
	s_lshl_b32 s8, s15, 7
	v_bitop3_b32 v166, v13, s8, v12 bitop3:0xde
	s_add_u32 s8, s10, 0x65640000
	v_bitop3_b32 v19, v13, s9, v12 bitop3:0xde
	s_addc_u32 s9, s11, 0
	s_add_u32 s10, s10, 0x77640000
	v_mov_b32_e32 v153, v128
	s_addc_u32 s11, s11, 0
	s_add_i32 s22, s14, 0x18000
	v_lshl_add_u64 v[14:15], v[0:1], 0, v[152:153]
	v_mov_b32_e32 v149, v128
	s_add_i32 s84, s22, s1
	v_lshl_add_u64 v[16:17], v[0:1], 0, v[148:149]
	v_lshl_add_u64 v[12:13], v[14:15], 0, s[40:41]
	s_mov_b32 m0, s84
	s_add_i32 s85, s84, 0x2000
	global_load_lds_dwordx4 v[12:13], off
	v_lshl_add_u64 v[12:13], v[16:17], 0, s[40:41]
	s_mov_b32 m0, s85
	s_add_i32 s86, s74, 0x8000
	global_load_lds_dwordx4 v[12:13], off
	v_lshl_add_u64 v[2:3], v[2:3], 0, s[40:41]
	s_mov_b32 m0, s86
	s_add_i32 s87, s74, 0xa000
	s_add_i32 s78, s14, 0x1c000
	global_load_lds_dwordx4 v[2:3], off
	v_lshl_add_u64 v[2:3], v[4:5], 0, s[40:41]
	s_mov_b32 m0, s87
	s_mov_b64 s[42:43], 0x20080
	global_load_lds_dwordx4 v[2:3], off
	v_lshl_add_u64 v[2:3], v[0:1], 0, s[42:43]
	s_add_i32 s88, s78, s1
	v_lshl_add_u64 v[4:5], v[2:3], 0, v[152:153]
	s_mov_b32 m0, s88
	s_add_i32 s89, s88, 0x2000
	global_load_lds_dwordx4 v[4:5], off
	v_lshl_add_u64 v[2:3], v[2:3], 0, v[148:149]
	s_mov_b32 m0, s89
	s_add_i32 s79, s14, 0x10800
	global_load_lds_dwordx4 v[2:3], off
	s_waitcnt vmcnt(8)
	s_barrier
	v_lshlrev_b32_e32 v2, 13, v10
	v_and_b32_e32 v2, 0xffffc000, v2
	v_lshl_add_u32 v2, v9, 10, v2
	v_and_b32_e32 v3, 1, v10
	v_lshl_or_b32 v2, v3, 6, v2
	v_lshl_add_u32 v156, v11, 1, v2
	v_lshlrev_b32_e32 v2, 13, v6
	v_and_b32_e32 v2, 0xffffc000, v2
	s_add_i32 s80, s14, 0x14800
	s_add_i32 s81, s14, 0x18800
	s_add_i32 s82, s14, 0x1c800
	s_ashr_i32 s83, s26, 31
	s_waitcnt vmcnt(6)
	v_lshl_add_u32 v2, v7, 10, v2
	v_and_b32_e32 v3, 1, v6
	s_cmpk_lt_u32 s0, 0x100
	v_lshl_or_b32 v2, v3, 6, v2
	v_or_b32_e32 v167, 0x400, v166
	s_cselect_b64 s[12:13], -1, 0
	v_ashrrev_i32_e32 v147, 31, v146
	v_or_b32_e32 v168, s15, v18
	v_mov_b32_e32 v157, v128
	v_lshl_add_u32 v158, v8, 1, v2
	v_mov_b32_e32 v159, v128
	s_mov_b32 s90, 0
	v_add_u32_e32 v169, s14, v19
	v_mov_b64_e32 v[162:163], v[0:1]
	s_mov_b64 s[70:71], s[20:21]
	s_barrier
	s_branch .LBB0_3421
